# grid barriers: the arriving workgroup invalidates its L1 right behind its arrival (it reads nothing another workgroup writes until the barrier completes) instead of after the wait
# speedup vs baseline: 1.0230x; 1.0114x over previous
; __device__ __forceinline__ unsigned xb_ld(unsigned* p)              { return __hip_atomic_load(p, __ATOMIC_RELAXED, __HIP_MEMORY_SCOPE_AGENT); }
; __device__ __forceinline__ unsigned xb_add(unsigned* p, unsigned v) { return __hip_atomic_fetch_add(p, v, __ATOMIC_RELAXED, __HIP_MEMORY_SCOPE_AGENT); }
; #define XB_SPIN(cond, bar) do { unsigned _sp = 0; while (cond) { __builtin_amdgcn_s_sleep(1); \
;     if ((++_sp & 255u) == 0u) { if (xb_ld(&(bar)[XB_TMO])) break; if (_sp > XB_SPIN_CAP) { atomicAdd(&(bar)[XB_TMO], 1u); break; } } } } while (0)
; __device__ __forceinline__ void xcd_barrier(const XcdBarrier& b, const int tid) {
;     ...
;         const unsigned old = xb_add(&bar[XB_XSUB(b.x)], 1u);
;         const unsigned gen = old / nloc;
;         if (old + 1u == (gen + 1u) * nloc) {
;             __builtin_amdgcn_fence(__ATOMIC_RELEASE, "agent");
;             asm volatile("s_waitcnt vmcnt(0)" ::: "memory");
;             const unsigned og = xb_add(&bar[XB_TOP], 1u);
;             const unsigned tg = og / nx;
;             if (og + 1u == (tg + 1u) * nx) xb_add(&bar[XB_TOPGEN], 1u);
;             else XB_SPIN(xb_ld(&bar[XB_TOPGEN]) == tg, bar);
.LBB0_79:
	s_or_b64 exec, exec, s[16:17]
	buffer_inv sc1
	v_cvt_f32_u32_e32 v4, v2
	s_waitcnt vmcnt(0)
	v_readfirstlane_b32 s12, v3
	v_sub_u32_e32 v3, 0, v2
	v_rcp_iflag_f32_e32 v4, v4
	v_add_u32_e32 v5, s12, v1
	v_mul_f32_e32 v4, 0x4f7ffffe, v4
	v_cvt_u32_f32_e32 v4, v4
	v_mul_lo_u32 v1, v3, v4
	v_mul_hi_u32 v1, v4, v1
	v_add_u32_e32 v1, v4, v1
	v_mul_hi_u32 v1, v5, v1
	v_mul_lo_u32 v3, v1, v2
	v_sub_u32_e32 v3, v5, v3
	v_add_u32_e32 v4, 1, v1
	v_cmp_ge_u32_e32 vcc, v3, v2
	s_nop 1
	v_cndmask_b32_e32 v1, v1, v4, vcc
	v_sub_u32_e32 v4, v3, v2
	v_cndmask_b32_e32 v3, v3, v4, vcc
	v_add_u32_e32 v4, 1, v1
	v_cmp_ge_u32_e32 vcc, v3, v2
	v_add_u32_e32 v3, 1, v5
	s_nop 0
	v_cndmask_b32_e32 v1, v1, v4, vcc
	v_mul_lo_u32 v4, v2, v1
	v_add_u32_e32 v2, v4, v2
	s_waitcnt lgkmcnt(0)
	v_add_u32_e32 v4, 1, v1
	v_mul_lo_u32 v4, v4, v0
	v_mov_b32_e32 v5, 0x3000
	v_cmp_ne_u32_e32 vcc, v3, v2
	s_cbranch_vccnz .Lgb0_wait
	buffer_wbl2 sc1
	s_waitcnt vmcnt(0) lgkmcnt(0)
	v_mov_b32_e32 v2, 1
	global_atomic_add v5, v2, s[26:27] offset:1024

; __device__ __forceinline__ unsigned xb_ld(unsigned* p)              { return __hip_atomic_load(p, __ATOMIC_RELAXED, __HIP_MEMORY_SCOPE_AGENT); }
; #define XB_SPIN(cond, bar) do { unsigned _sp = 0; while (cond) { __builtin_amdgcn_s_sleep(1); \
;     if ((++_sp & 255u) == 0u) { if (xb_ld(&(bar)[XB_TMO])) break; if (_sp > XB_SPIN_CAP) { atomicAdd(&(bar)[XB_TMO], 1u); break; } } } } while (0)
; __device__ __forceinline__ void xcd_barrier(const XcdBarrier& b, const int tid) {
;     ...
;             else XB_SPIN(xb_ld(&bar[XB_TOPGEN]) == tg, bar);
;             __builtin_amdgcn_fence(__ATOMIC_ACQUIRE, "agent");
.Lgb0_done:
.Lgb0_out:
	s_waitcnt vmcnt(0)

; __device__ __forceinline__ unsigned xb_add(unsigned* p, unsigned v) { return __hip_atomic_fetch_add(p, v, __ATOMIC_RELAXED, __HIP_MEMORY_SCOPE_AGENT); }
; __device__ __forceinline__ void xcd_barrier(const XcdBarrier& b, const int tid) {
;     ...
;         const unsigned old = xb_add(&bar[XB_XSUB(b.x)], 1u);
;         const unsigned gen = old / nloc;
;         if (old + 1u == (gen + 1u) * nloc) {
;             __builtin_amdgcn_fence(__ATOMIC_RELEASE, "agent");
;             asm volatile("s_waitcnt vmcnt(0)" ::: "memory");
;             const unsigned og = xb_add(&bar[XB_TOP], 1u);
;             const unsigned tg = og / nx;
;             if (og + 1u == (tg + 1u) * nx) xb_add(&bar[XB_TOPGEN], 1u);
.LBB0_169:
	s_or_b64 exec, exec, s[22:23]
	buffer_inv sc1
	v_cvt_f32_u32_e32 v4, v2
	s_waitcnt vmcnt(0)
	v_readfirstlane_b32 s20, v3
	v_sub_u32_e32 v3, 0, v2
	v_rcp_iflag_f32_e32 v4, v4
	v_add_u32_e32 v5, s20, v1
	v_mul_f32_e32 v4, 0x4f7ffffe, v4
	v_cvt_u32_f32_e32 v4, v4
	v_mul_lo_u32 v1, v3, v4
	v_mul_hi_u32 v1, v4, v1
	v_add_u32_e32 v1, v4, v1
	v_mul_hi_u32 v1, v5, v1
	v_mul_lo_u32 v3, v1, v2
	v_sub_u32_e32 v3, v5, v3
	v_add_u32_e32 v4, 1, v1
	v_cmp_ge_u32_e32 vcc, v3, v2
	s_nop 1
	v_cndmask_b32_e32 v1, v1, v4, vcc
	v_sub_u32_e32 v4, v3, v2
	v_cndmask_b32_e32 v3, v3, v4, vcc
	v_add_u32_e32 v4, 1, v1
	v_cmp_ge_u32_e32 vcc, v3, v2
	v_add_u32_e32 v3, 1, v5
	s_nop 0
	v_cndmask_b32_e32 v1, v1, v4, vcc
	v_mul_lo_u32 v4, v2, v1
	v_add_u32_e32 v2, v4, v2
	s_waitcnt lgkmcnt(0)
	v_add_u32_e32 v4, 1, v1
	v_mul_lo_u32 v4, v4, v0
	v_mov_b32_e32 v5, 0x3000
	v_cmp_ne_u32_e32 vcc, v3, v2
	s_cbranch_vccnz .Lgb1_out
	buffer_wbl2 sc1
	s_waitcnt vmcnt(0) lgkmcnt(0)
	v_mov_b32_e32 v2, 1
	global_atomic_add v5, v2, s[26:27] offset:1024

; __device__ __forceinline__ unsigned xb_ld(unsigned* p)              { return __hip_atomic_load(p, __ATOMIC_RELAXED, __HIP_MEMORY_SCOPE_AGENT); }
; #define XB_SPIN(cond, bar) do { unsigned _sp = 0; while (cond) { __builtin_amdgcn_s_sleep(1); \
;     if ((++_sp & 255u) == 0u) { if (xb_ld(&(bar)[XB_TMO])) break; if (_sp > XB_SPIN_CAP) { atomicAdd(&(bar)[XB_TMO], 1u); break; } } } } while (0)
; __device__ __forceinline__ void xcd_barrier(const XcdBarrier& b, const int tid) {
;     ...
;             XB_SPIN(xb_ld(&bar[XB_XGEN(b.x)]) == gen, bar);
;             __builtin_amdgcn_fence(__ATOMIC_ACQUIRE, "agent");
;             asm volatile("s_waitcnt vmcnt(0)" ::: "memory");
.Lp2gb_lead_done:
	v_mov_b32_e32 v21, 0x22610
	v_mov_b32_e32 v22, 1
	s_waitcnt vmcnt(0)
	ds_write_b32 v21, v22
	s_waitcnt lgkmcnt(0)
	s_branch .Lp2gb_done

; __device__ __forceinline__ unsigned xb_ld(unsigned* p)              { return __hip_atomic_load(p, __ATOMIC_RELAXED, __HIP_MEMORY_SCOPE_AGENT); }
; __device__ __forceinline__ unsigned xb_add(unsigned* p, unsigned v) { return __hip_atomic_fetch_add(p, v, __ATOMIC_RELAXED, __HIP_MEMORY_SCOPE_AGENT); }
; #define XB_SPIN(cond, bar) do { unsigned _sp = 0; while (cond) { __builtin_amdgcn_s_sleep(1); \
;     if ((++_sp & 255u) == 0u) { if (xb_ld(&(bar)[XB_TMO])) break; if (_sp > XB_SPIN_CAP) { atomicAdd(&(bar)[XB_TMO], 1u); break; } } } } while (0)
; __device__ __forceinline__ void xcd_barrier(const XcdBarrier& b, const int tid) {
;     ...
;         const unsigned old = xb_add(&bar[XB_XSUB(b.x)], 1u);
;         const unsigned gen = old / nloc;
;         if (old + 1u == (gen + 1u) * nloc) {
;             __builtin_amdgcn_fence(__ATOMIC_RELEASE, "agent");
;             asm volatile("s_waitcnt vmcnt(0)" ::: "memory");
;             const unsigned og = xb_add(&bar[XB_TOP], 1u);
;             const unsigned tg = og / nx;
;             if (og + 1u == (tg + 1u) * nx) xb_add(&bar[XB_TOPGEN], 1u);
;             else XB_SPIN(xb_ld(&bar[XB_TOPGEN]) == tg, bar);
.LBB0_433:
	s_or_b64 exec, exec, s[12:13]
	buffer_inv sc1
	v_cvt_f32_u32_e32 v4, v2
	s_waitcnt vmcnt(0)
	v_readfirstlane_b32 s6, v3
	v_sub_u32_e32 v3, 0, v2
	v_rcp_iflag_f32_e32 v4, v4
	v_add_u32_e32 v5, s6, v1
	v_mul_f32_e32 v4, 0x4f7ffffe, v4
	v_cvt_u32_f32_e32 v4, v4
	v_mul_lo_u32 v1, v3, v4
	v_mul_hi_u32 v1, v4, v1
	v_add_u32_e32 v1, v4, v1
	v_mul_hi_u32 v1, v5, v1
	v_mul_lo_u32 v3, v1, v2
	v_sub_u32_e32 v3, v5, v3
	v_add_u32_e32 v4, 1, v1
	v_cmp_ge_u32_e32 vcc, v3, v2
	s_nop 1
	v_cndmask_b32_e32 v1, v1, v4, vcc
	v_sub_u32_e32 v4, v3, v2
	v_cndmask_b32_e32 v3, v3, v4, vcc
	v_add_u32_e32 v4, 1, v1
	v_cmp_ge_u32_e32 vcc, v3, v2
	v_add_u32_e32 v3, 1, v5
	s_nop 0
	v_cndmask_b32_e32 v1, v1, v4, vcc
	v_mul_lo_u32 v4, v2, v1
	v_add_u32_e32 v2, v4, v2
	s_waitcnt lgkmcnt(0)
	v_add_u32_e32 v4, 1, v1
	v_mul_lo_u32 v4, v4, v0
	v_mov_b32_e32 v5, 0x3000
	v_cmp_ne_u32_e32 vcc, v3, v2
	s_cbranch_vccnz .Lgb2_wait
	buffer_wbl2 sc1
	s_waitcnt vmcnt(0) lgkmcnt(0)
	v_mov_b32_e32 v2, 1
	global_atomic_add v5, v2, s[26:27] offset:1024

; __device__ __forceinline__ unsigned xb_ld(unsigned* p)              { return __hip_atomic_load(p, __ATOMIC_RELAXED, __HIP_MEMORY_SCOPE_AGENT); }
; __device__ __forceinline__ unsigned xb_add(unsigned* p, unsigned v) { return __hip_atomic_fetch_add(p, v, __ATOMIC_RELAXED, __HIP_MEMORY_SCOPE_AGENT); }
; #define XB_SPIN(cond, bar) do { unsigned _sp = 0; while (cond) { __builtin_amdgcn_s_sleep(1); \
;     if ((++_sp & 255u) == 0u) { if (xb_ld(&(bar)[XB_TMO])) break; if (_sp > XB_SPIN_CAP) { atomicAdd(&(bar)[XB_TMO], 1u); break; } } } } while (0)
; __device__ __forceinline__ void xcd_barrier(const XcdBarrier& b, const int tid) {
;     ...
;         const unsigned old = xb_add(&bar[XB_XSUB(b.x)], 1u);
;         const unsigned gen = old / nloc;
;         if (old + 1u == (gen + 1u) * nloc) {
;             __builtin_amdgcn_fence(__ATOMIC_RELEASE, "agent");
;             asm volatile("s_waitcnt vmcnt(0)" ::: "memory");
;             const unsigned og = xb_add(&bar[XB_TOP], 1u);
;             const unsigned tg = og / nx;
;             if (og + 1u == (tg + 1u) * nx) xb_add(&bar[XB_TOPGEN], 1u);
;             else XB_SPIN(xb_ld(&bar[XB_TOPGEN]) == tg, bar);
.LBB0_512:
	s_or_b64 exec, exec, s[8:9]
	buffer_inv sc1
	v_cvt_f32_u32_e32 v4, v2
	s_waitcnt vmcnt(0)
	v_readfirstlane_b32 s6, v3
	v_sub_u32_e32 v3, 0, v2
	v_rcp_iflag_f32_e32 v4, v4
	v_add_u32_e32 v5, s6, v1
	v_mul_f32_e32 v4, 0x4f7ffffe, v4
	v_cvt_u32_f32_e32 v4, v4
	v_mul_lo_u32 v1, v3, v4
	v_mul_hi_u32 v1, v4, v1
	v_add_u32_e32 v1, v4, v1
	v_mul_hi_u32 v1, v5, v1
	v_mul_lo_u32 v3, v1, v2
	v_sub_u32_e32 v3, v5, v3
	v_add_u32_e32 v4, 1, v1
	v_cmp_ge_u32_e32 vcc, v3, v2
	s_nop 1
	v_cndmask_b32_e32 v1, v1, v4, vcc
	v_sub_u32_e32 v4, v3, v2
	v_cndmask_b32_e32 v3, v3, v4, vcc
	v_add_u32_e32 v4, 1, v1
	v_cmp_ge_u32_e32 vcc, v3, v2
	v_add_u32_e32 v3, 1, v5
	s_nop 0
	v_cndmask_b32_e32 v1, v1, v4, vcc
	v_mul_lo_u32 v4, v2, v1
	v_add_u32_e32 v2, v4, v2
	s_waitcnt lgkmcnt(0)
	v_add_u32_e32 v4, 1, v1
	v_mul_lo_u32 v4, v4, v0
	v_mov_b32_e32 v5, 0x3000
	v_cmp_ne_u32_e32 vcc, v3, v2
	s_cbranch_vccnz .Lgb3_wait
	buffer_wbl2 sc1
	s_waitcnt vmcnt(0) lgkmcnt(0)
	v_mov_b32_e32 v2, 1
	global_atomic_add v5, v2, s[26:27] offset:1024

; __device__ __forceinline__ unsigned xb_ld(unsigned* p)              { return __hip_atomic_load(p, __ATOMIC_RELAXED, __HIP_MEMORY_SCOPE_AGENT); }
; __device__ __forceinline__ unsigned xb_add(unsigned* p, unsigned v) { return __hip_atomic_fetch_add(p, v, __ATOMIC_RELAXED, __HIP_MEMORY_SCOPE_AGENT); }
; #define XB_SPIN(cond, bar) do { unsigned _sp = 0; while (cond) { __builtin_amdgcn_s_sleep(1); \
;     if ((++_sp & 255u) == 0u) { if (xb_ld(&(bar)[XB_TMO])) break; if (_sp > XB_SPIN_CAP) { atomicAdd(&(bar)[XB_TMO], 1u); break; } } } } while (0)
; __device__ __forceinline__ void xcd_barrier(const XcdBarrier& b, const int tid) {
;     ...
;         const unsigned old = xb_add(&bar[XB_XSUB(b.x)], 1u);
;         const unsigned gen = old / nloc;
;         if (old + 1u == (gen + 1u) * nloc) {
;             __builtin_amdgcn_fence(__ATOMIC_RELEASE, "agent");
;             asm volatile("s_waitcnt vmcnt(0)" ::: "memory");
;             const unsigned og = xb_add(&bar[XB_TOP], 1u);
;             const unsigned tg = og / nx;
;             if (og + 1u == (tg + 1u) * nx) xb_add(&bar[XB_TOPGEN], 1u);
;             else XB_SPIN(xb_ld(&bar[XB_TOPGEN]) == tg, bar);
;             __builtin_amdgcn_fence(__ATOMIC_ACQUIRE, "agent");
;             xb_add(&bar[XB_XGEN(b.x)], 1u);
;             asm volatile("s_waitcnt vmcnt(0)" ::: "memory");
.LBB0_802:
	s_or_b64 exec, exec, s[10:11]
	buffer_inv sc1
	v_cvt_f32_u32_e32 v4, v2
	s_waitcnt vmcnt(0)
	v_readfirstlane_b32 s8, v3
	v_sub_u32_e32 v3, 0, v2
	v_rcp_iflag_f32_e32 v4, v4
	v_add_u32_e32 v5, s8, v1
	v_mul_f32_e32 v4, 0x4f7ffffe, v4
	v_cvt_u32_f32_e32 v4, v4
	v_mul_lo_u32 v1, v3, v4
	v_mul_hi_u32 v1, v4, v1
	v_add_u32_e32 v1, v4, v1
	v_mul_hi_u32 v1, v5, v1
	v_mul_lo_u32 v3, v1, v2
	v_sub_u32_e32 v3, v5, v3
	v_add_u32_e32 v4, 1, v1
	v_cmp_ge_u32_e32 vcc, v3, v2
	s_nop 1
	v_cndmask_b32_e32 v1, v1, v4, vcc
	v_sub_u32_e32 v4, v3, v2
	v_cndmask_b32_e32 v3, v3, v4, vcc
	v_add_u32_e32 v4, 1, v1
	v_cmp_ge_u32_e32 vcc, v3, v2
	v_add_u32_e32 v3, 1, v5
	s_nop 0
	v_cndmask_b32_e32 v1, v1, v4, vcc
	v_mul_lo_u32 v4, v2, v1
	v_add_u32_e32 v2, v4, v2
	s_waitcnt lgkmcnt(0)
	v_add_u32_e32 v4, 1, v1
	v_mul_lo_u32 v4, v4, v0
	v_mov_b32_e32 v5, 0x3000
	v_cmp_ne_u32_e32 vcc, v3, v2
	s_cbranch_vccnz .Lgb5_wait
	buffer_wbl2 sc1
	s_waitcnt vmcnt(0) lgkmcnt(0)
	v_mov_b32_e32 v2, 1
	global_atomic_add v5, v2, s[26:27] offset:1024

; __device__ __forceinline__ unsigned xb_ld(unsigned* p)              { return __hip_atomic_load(p, __ATOMIC_RELAXED, __HIP_MEMORY_SCOPE_AGENT); }
; #define XB_SPIN(cond, bar) do { unsigned _sp = 0; while (cond) { __builtin_amdgcn_s_sleep(1); \
;     if ((++_sp & 255u) == 0u) { if (xb_ld(&(bar)[XB_TMO])) break; if (_sp > XB_SPIN_CAP) { atomicAdd(&(bar)[XB_TMO], 1u); break; } } } } while (0)
; __device__ __forceinline__ void xcd_barrier(const XcdBarrier& b, const int tid) {
;     ...
;             XB_SPIN(xb_ld(&bar[XB_XGEN(b.x)]) == gen, bar);
;             __builtin_amdgcn_fence(__ATOMIC_ACQUIRE, "agent");
;             asm volatile("s_waitcnt vmcnt(0)" ::: "memory");
;         }
;     }
;     __syncthreads();
.Lp7gb_lead_done:
	v_mov_b32_e32 v100, 0x22614
	v_mov_b32_e32 v102, 1
	s_waitcnt vmcnt(0)
	ds_write_b32 v100, v102
	s_waitcnt lgkmcnt(0)
	s_branch .Lp7gb_done
